# banded attention loops: Q fragment loads waited once before the tile loop; in-loop waits no longer wait for the next tile's loads
# speedup vs baseline: 1.0136x; 1.0042x over previous
.LBB0_453:
	s_ashr_i32 s8, s20, 6
	s_mul_hi_i32 s9, s8, 0x55555556
	s_lshr_b32 s11, s9, 31
	s_add_i32 s9, s9, s11
	s_mul_i32 s9, s9, 3
	s_sub_i32 s26, s8, s9
	s_mul_hi_i32 s8, s20, 0x2aaaaaab
	s_lshr_b32 s9, s8, 31
	s_lshr_b32 s8, s8, 5
	s_and_b32 s10, s20, 15
	s_bfe_u32 s29, s20, 0x20004
	s_add_i32 s11, s8, s9
	s_cmp_lg_u32 s26, 1
	s_cselect_b64 s[8:9], -1, 0
	s_cmp_eq_u32 s26, 1
	s_mov_b32 s13, 0xb800
	s_cselect_b32 s12, 2, 4
	s_cselect_b32 s28, s13, 0x2e000
	s_cmp_eq_u32 s26, 0
	s_cselect_b32 s12, 0, s12
	s_cselect_b32 s30, 0x2e00, s28
	s_lshr_b32 s14, 16, s12
	s_add_i32 s14, s14, -1
	s_sub_i32 s15, 4, s12
	s_and_b32 s76, s14, s10
	s_lshr_b32 s13, 0x1000, s12
	s_lshr_b32 s15, s10, s15
	s_lshl_b32 s36, s76, 8
	s_lshr_b32 s10, 64, s12
	s_cmp_gt_u32 s12, 3
	s_cselect_b32 s34, s10, 6
	v_sub_u32_e64 v2, s36, 64 clamp
	s_lshl_b32 s10, s34, 6
	s_sub_i32 s10, s13, s10
	v_readfirstlane_b32 s13, v2
	s_min_i32 s35, s13, s10
	s_lshl_b32 s10, s11, 12
	s_or_b32 s13, s15, s10
	s_mul_i32 s14, s13, 0x5c00
	s_mul_hi_i32 s11, s13, 0x5c00
	s_mul_i32 s10, s26, 0x600
	s_add_u32 s14, s46, s14
	s_addc_u32 s15, s47, s11
	s_ashr_i32 s11, s10, 31
	s_lshl_b64 s[10:11], s[10:11], 1
	s_add_u32 s10, s14, s10
	s_addc_u32 s11, s15, s11
	s_lshl_b32 s14, s29, 8
	s_add_u32 s77, s10, s14
	s_addc_u32 s78, s11, 0
	s_ashr_i32 s27, s26, 31
	s_lshl_b64 s[10:11], s[26:27], 23
	s_add_u32 s15, s48, s10
	s_addc_u32 s31, s49, s11
	s_lshl_b32 s10, s36, s12
	s_add_i32 s12, s10, s13
	s_ashr_i32 s13, s12, 31
	s_lshl_b64 s[10:11], s[12:13], 10
	s_add_u32 s10, s15, s10
	s_addc_u32 s11, s31, s11
	s_add_u32 s10, s10, s14
	s_addc_u32 s11, s11, 0
	s_lshl_b64 s[14:15], s[26:27], 17
	s_add_u32 s14, s50, s14
	s_addc_u32 s15, s51, s15
	s_lshl_b64 s[12:13], s[12:13], 4
	s_add_u32 s12, s14, s12
	s_addc_u32 s13, s15, s13
	s_lshl_b32 s14, s29, 2
	s_add_u32 s12, s12, s14
	s_mul_hi_i32 s15, s35, s30
	s_mul_i32 s14, s35, s30
	s_addc_u32 s13, s13, 0
	s_lshl_b64 s[14:15], s[14:15], 1
	s_add_u32 s14, s77, s14
	s_addc_u32 s15, s78, s15
	s_sub_i32 s37, s36, s35
	s_cmp_lg_u32 s26, 0
	s_mov_b64 s[26:27], -1
	s_cbranch_scc0 .LBB0_470
	s_mul_i32 s26, s36, s28
	s_lshl_b32 s26, s26, 1
	s_add_u32 s26, s77, s26
	s_addc_u32 s27, s78, 0
	s_mov_b64 s[28:29], -1
	s_and_b64 vcc, exec, s[8:9]
	s_cbranch_vccz .LBB0_476
	global_load_dwordx4 v[114:117], v213, s[26:27]
	global_load_dwordx4 v[118:121], v213, s[26:27] offset:32
	v_lshl_add_u64 v[184:185], s[14:15], 0, v[166:167]
	v_add_co_u32_e32 v4, vcc, 0xb80000, v184
	v_add_u32_e32 v50, 0, v165
	s_nop 0
	v_addc_co_u32_e32 v5, vcc, 0, v185, vcc
	global_load_dwordx4 v[130:133], v[184:185], off offset:2048
	global_load_dwordx4 v[150:153], v[184:185], off offset:1024
	global_load_dwordx4 v[154:157], v[4:5], off offset:2048
	global_load_dwordx4 v[158:161], v[4:5], off offset:1024
	global_load_dwordx4 v[122:125], v213, s[26:27] offset:64
	global_load_dwordx4 v[126:129], v213, s[26:27] offset:96
	global_load_dwordx4 v[134:137], v213, s[26:27] offset:128
	global_load_dwordx4 v[138:141], v213, s[26:27] offset:160
	global_load_dwordx4 v[142:145], v213, s[26:27] offset:192
	global_load_dwordx4 v[146:149], v213, s[26:27] offset:224
	v_add_u32_e32 v51, 0, v196
	v_add_u32_e32 v52, 0, v197
	v_add_u32_e32 v53, 0, v198
	v_add_u32_e32 v18, s36, v211
	v_mov_b32_e32 v16, v3
	v_mov_b32_e32 v17, v3
	v_add_u32_e32 v175, s37, v1
	v_mov_b32_e32 v2, v3
	v_mov_b32_e32 v4, v3
	v_mov_b32_e32 v5, v3
	v_mov_b32_e32 v6, v3
	v_mov_b32_e32 v7, v3
	v_mov_b32_e32 v8, v3
	v_mov_b32_e32 v9, v3
	v_mov_b32_e32 v10, v3
	v_mov_b32_e32 v11, v3
	v_mov_b32_e32 v12, v3
	v_mov_b32_e32 v13, v3
	v_mov_b32_e32 v14, v3
	v_mov_b32_e32 v15, v3
	v_subrev_u32_e32 v179, s35, v18
	v_mov_b64_e32 v[80:81], v[16:17]
	v_mov_b64_e32 v[48:49], v[16:17]
	v_mov_b64_e32 v[32:33], v[16:17]
	s_mov_b32 s8, 0
	v_mov_b32_e32 v181, 0
	v_mov_b32_e32 v173, 0xf149f2ca
	s_movk_i32 s79, 0x7f
	v_add_u32_e32 v177, 0x5f, v175
	v_mov_b64_e32 v[78:79], v[14:15]
	v_mov_b64_e32 v[76:77], v[12:13]
	v_mov_b64_e32 v[74:75], v[10:11]
	v_mov_b64_e32 v[72:73], v[8:9]
	v_mov_b64_e32 v[70:71], v[6:7]
	v_mov_b64_e32 v[68:69], v[4:5]
	v_mov_b64_e32 v[66:67], v[2:3]
	v_mov_b64_e32 v[46:47], v[14:15]
	v_mov_b64_e32 v[44:45], v[12:13]
	v_mov_b64_e32 v[42:43], v[10:11]
	v_mov_b64_e32 v[40:41], v[8:9]
	v_mov_b64_e32 v[38:39], v[6:7]
	v_mov_b64_e32 v[36:37], v[4:5]
	v_mov_b64_e32 v[34:35], v[2:3]
	v_mov_b64_e32 v[30:31], v[14:15]
	v_mov_b64_e32 v[28:29], v[12:13]
	v_mov_b64_e32 v[26:27], v[10:11]
	v_mov_b64_e32 v[24:25], v[8:9]
	v_mov_b64_e32 v[22:23], v[6:7]
	v_mov_b64_e32 v[20:21], v[4:5]
	v_mov_b64_e32 v[18:19], v[2:3]
	s_waitcnt vmcnt(9)
	ds_write_b128 v50, v[130:133]
	s_waitcnt vmcnt(7)
	ds_write_b128 v51, v[154:157]
	ds_write_b128 v52, v[150:153] offset:32768
	s_waitcnt vmcnt(6)
	ds_write_b128 v53, v[158:161] offset:32768
	v_mov_b64_e32 v[64:65], v[16:17]
	v_mov_b64_e32 v[62:63], v[14:15]
	v_mov_b64_e32 v[60:61], v[12:13]
	v_mov_b64_e32 v[58:59], v[10:11]
	v_mov_b64_e32 v[56:57], v[8:9]
	v_mov_b64_e32 v[54:55], v[6:7]
	v_mov_b64_e32 v[52:53], v[4:5]
	v_mov_b64_e32 v[50:51], v[2:3]
	s_waitcnt lgkmcnt(0)
	s_barrier
	s_waitcnt vmcnt(0)

.LBB0_458:
	s_and_b32 s81, s8, 1
	s_add_i32 s8, s79, 0xffffff81
	v_cmp_le_i32_e32 vcc, s8, v177
	v_cmp_ge_i32_e64 s[8:9], s79, v175
	s_and_b64 s[30:31], vcc, s[8:9]
	s_and_saveexec_b64 s[8:9], s[30:31]
	s_cbranch_execz .LBB0_465
	s_lshl_b32 s82, s81, 14
	s_add_i32 s30, s82, 0
	v_add3_u32 v2, s30, v200, v199
	ds_read_b128 v[4:7], v2 offset:32768
	ds_read_b128 v[224:227], v2 offset:40960
	v_add3_u32 v2, s30, v201, v199
	ds_read_b128 v[228:231], v2 offset:32768
	ds_read_b128 v[232:235], v2 offset:40960
	v_add_u32_e32 v11, 50, v179
	v_add_u32_e32 v13, 49, v179
	v_add_u32_e32 v15, 48, v179
	v_add_u32_e32 v17, 43, v179
	s_waitcnt lgkmcnt(3)
	v_mfma_f32_32x32x16_bf16 v[82:97], v[4:7], v[114:117], 0
	v_add3_u32 v2, s30, v202, v199
	ds_read_b128 v[4:7], v2 offset:32768
	s_waitcnt lgkmcnt(3)
	v_mfma_f32_32x32x16_bf16 v[98:113], v[224:227], v[114:117], 0
	ds_read_b128 v[224:227], v2 offset:40960
	s_waitcnt lgkmcnt(3)
	v_mfma_f32_32x32x16_bf16 v[82:97], v[228:231], v[118:121], v[82:97]
	v_add3_u32 v2, s30, v203, v199
	ds_read_b128 v[228:231], v2 offset:32768
	s_waitcnt lgkmcnt(3)
	v_mfma_f32_32x32x16_bf16 v[98:113], v[232:235], v[118:121], v[98:113]
	ds_read_b128 v[232:235], v2 offset:40960
	s_waitcnt lgkmcnt(3)
	v_mfma_f32_32x32x16_bf16 v[82:97], v[4:7], v[122:125], v[82:97]
	v_add3_u32 v2, s30, v204, v199
	ds_read_b128 v[4:7], v2 offset:32768
	s_waitcnt lgkmcnt(3)
	v_mfma_f32_32x32x16_bf16 v[98:113], v[224:227], v[122:125], v[98:113]
	ds_read_b128 v[224:227], v2 offset:40960
	s_waitcnt lgkmcnt(3)
	v_mfma_f32_32x32x16_bf16 v[82:97], v[228:231], v[126:129], v[82:97]
	v_add3_u32 v2, s30, v205, v199
	ds_read_b128 v[228:231], v2 offset:32768
	s_waitcnt lgkmcnt(3)
	v_mfma_f32_32x32x16_bf16 v[98:113], v[232:235], v[126:129], v[98:113]
	ds_read_b128 v[232:235], v2 offset:40960
	s_waitcnt lgkmcnt(3)
	v_mfma_f32_32x32x16_bf16 v[82:97], v[4:7], v[134:137], v[82:97]
	v_add3_u32 v2, s30, v206, v199
	ds_read_b128 v[4:7], v2 offset:32768
	s_waitcnt lgkmcnt(3)
	v_mfma_f32_32x32x16_bf16 v[98:113], v[224:227], v[134:137], v[98:113]
	ds_read_b128 v[224:227], v2 offset:40960
	s_waitcnt lgkmcnt(3)
	v_mfma_f32_32x32x16_bf16 v[82:97], v[228:231], v[138:141], v[82:97]
	v_add3_u32 v2, s30, v207, v199
	ds_read_b128 v[228:231], v2 offset:32768
	s_waitcnt lgkmcnt(3)
	v_mfma_f32_32x32x16_bf16 v[98:113], v[232:235], v[138:141], v[98:113]
	ds_read_b128 v[232:235], v2 offset:40960
	s_waitcnt lgkmcnt(3)
	v_mfma_f32_32x32x16_bf16 v[82:97], v[4:7], v[142:145], v[82:97]
	s_waitcnt lgkmcnt(2)
	v_mfma_f32_32x32x16_bf16 v[98:113], v[224:227], v[142:145], v[98:113]
	s_waitcnt lgkmcnt(1)
	v_mfma_f32_32x32x16_bf16 v[82:97], v[228:231], v[146:149], v[82:97]
	v_add_u32_e32 v2, 59, v179
	v_cmp_lt_u32_e32 vcc, s55, v2
	v_add_u32_e32 v2, 27, v179
	v_add_u32_e32 v4, 58, v179
	s_nop 7
	v_cndmask_b32_e32 v5, v220, v82, vcc
	s_waitcnt lgkmcnt(0)
	v_mfma_f32_32x32x16_bf16 v[98:113], v[232:235], v[146:149], v[98:113]
	v_cmp_lt_u32_e32 vcc, s55, v2
	v_add_u32_e32 v6, 57, v179
	v_add_u32_e32 v7, 56, v179
	v_add_u32_e32 v9, 51, v179
	s_nop 7
	v_cndmask_b32_e32 v2, v220, v98, vcc
	v_cmp_lt_u32_e32 vcc, s55, v4
	v_add_u32_e32 v4, 26, v179
	s_nop 0
	v_cndmask_b32_e32 v8, v220, v83, vcc
	v_cmp_lt_u32_e32 vcc, s55, v4
	s_nop 1
	v_cndmask_b32_e32 v4, v220, v99, vcc
	v_cmp_lt_u32_e32 vcc, s55, v6
	v_add_u32_e32 v6, 25, v179
	s_nop 0
	v_cndmask_b32_e32 v10, v220, v84, vcc
	v_cmp_lt_u32_e32 vcc, s55, v6
	s_nop 1
	v_cndmask_b32_e32 v6, v220, v100, vcc
	v_cmp_lt_u32_e32 vcc, s55, v7
	v_add_u32_e32 v7, 24, v179
	v_max_f32_e32 v100, v5, v5
	v_cndmask_b32_e32 v12, v220, v85, vcc
	v_cmp_lt_u32_e32 vcc, s55, v7
	s_nop 1
	v_cndmask_b32_e32 v7, v220, v101, vcc
	v_cmp_lt_u32_e32 vcc, s55, v9
	v_add_u32_e32 v9, 19, v179
	s_nop 0
	v_cndmask_b32_e32 v14, v220, v86, vcc
	v_cmp_lt_u32_e32 vcc, s55, v9
	s_nop 1
	v_cndmask_b32_e32 v9, v220, v102, vcc
	v_cmp_lt_u32_e32 vcc, s55, v11
	v_add_u32_e32 v11, 18, v179
	s_nop 0
	v_cndmask_b32_e32 v16, v220, v87, vcc
	v_cmp_lt_u32_e32 vcc, s55, v11
	s_nop 1
	v_cndmask_b32_e32 v11, v220, v103, vcc
	v_cmp_lt_u32_e32 vcc, s55, v13
	v_add_u32_e32 v13, 17, v179
	s_nop 0
	v_cndmask_b32_e32 v83, v220, v88, vcc
	v_cmp_lt_u32_e32 vcc, s55, v13
	s_nop 1
	v_cndmask_b32_e32 v13, v220, v104, vcc
	v_cmp_lt_u32_e32 vcc, s55, v15
	v_add_u32_e32 v15, 16, v179
	s_nop 0
	v_cndmask_b32_e32 v85, v220, v89, vcc
	v_cmp_lt_u32_e32 vcc, s55, v15
	s_nop 1
	v_cndmask_b32_e32 v15, v220, v105, vcc
	v_cmp_lt_u32_e32 vcc, s55, v17
	v_add_u32_e32 v17, 11, v179
	s_nop 0
	v_cndmask_b32_e32 v87, v220, v90, vcc
	v_cmp_lt_u32_e32 vcc, s55, v17
	v_add_u32_e32 v17, 42, v179
	s_nop 0
	v_cndmask_b32_e32 v82, v220, v106, vcc
	v_cmp_lt_u32_e32 vcc, s55, v17
	v_add_u32_e32 v17, 10, v179
	s_nop 0
	v_cndmask_b32_e32 v89, v220, v91, vcc
	v_cmp_lt_u32_e32 vcc, s55, v17
	v_add_u32_e32 v17, 41, v179
	s_nop 0
	v_cndmask_b32_e32 v84, v220, v107, vcc
	v_cmp_lt_u32_e32 vcc, s55, v17
	v_add_u32_e32 v17, 9, v179
	s_nop 0
	v_cndmask_b32_e32 v91, v220, v92, vcc
	v_cmp_lt_u32_e32 vcc, s55, v17
	v_add_u32_e32 v17, 40, v179
	s_nop 0
	v_cndmask_b32_e32 v86, v220, v108, vcc
	v_cmp_lt_u32_e32 vcc, s55, v17
	v_add_u32_e32 v17, 8, v179
	s_nop 0
	v_cndmask_b32_e32 v93, v220, v93, vcc
	v_cmp_lt_u32_e32 vcc, s55, v17
	v_add_u32_e32 v17, 35, v179
	s_nop 0
	v_cndmask_b32_e32 v88, v220, v109, vcc
	v_cmp_lt_u32_e32 vcc, s55, v17
	v_add_u32_e32 v17, 3, v179
	s_nop 0
	v_cndmask_b32_e32 v98, v220, v94, vcc
	v_cmp_lt_u32_e32 vcc, s55, v17
	v_add_u32_e32 v17, 34, v179
	s_nop 0
	v_cndmask_b32_e32 v90, v220, v110, vcc
	v_cmp_lt_u32_e32 vcc, s55, v17
	v_add_u32_e32 v17, 2, v179
	s_nop 0
	v_cndmask_b32_e32 v99, v220, v95, vcc
	v_cmp_lt_u32_e32 vcc, s55, v17
	v_add_u32_e32 v17, 33, v179
	s_nop 0
	v_cndmask_b32_e32 v92, v220, v111, vcc
	v_cmp_lt_u32_e32 vcc, s55, v17
	v_add_u32_e32 v17, 1, v179
	s_nop 0
	v_cndmask_b32_e32 v96, v220, v96, vcc
	v_cmp_lt_u32_e32 vcc, s55, v17
	v_add_u32_e32 v17, 32, v179
	s_nop 0
	v_cndmask_b32_e32 v94, v220, v112, vcc
	v_cmp_lt_u32_e32 vcc, s55, v17
	v_max_f32_e32 v17, v8, v8
	v_max_f32_e32 v17, v100, v17
	v_max3_f32 v17, v17, v10, v12
	v_max3_f32 v17, v17, v14, v16
	v_max3_f32 v17, v17, v83, v85
	v_max3_f32 v17, v17, v87, v89
	v_max3_f32 v17, v17, v91, v93
	v_cndmask_b32_e32 v97, v220, v97, vcc
	v_max3_f32 v17, v17, v98, v99
	v_max3_f32 v17, v17, v96, v97
	v_max3_f32 v17, v17, v2, v4
	v_max3_f32 v17, v17, v6, v7
	v_max3_f32 v17, v17, v9, v11
	v_max3_f32 v17, v17, v13, v15
	v_max3_f32 v17, v17, v82, v84
	v_cmp_lt_u32_e32 vcc, s55, v179
	v_max3_f32 v17, v17, v86, v88
	v_max3_f32 v17, v17, v90, v92
	v_cndmask_b32_e32 v95, v220, v113, vcc
	v_max3_f32 v17, v17, v94, v95
	v_mov_b32_e32 v100, v17
	s_nop 1
	v_permlane32_swap_b32_e32 v17, v100
	v_max_f32_e32 v100, v100, v100
	v_max_f32_e32 v17, v17, v17
	v_max_f32_e32 v100, v17, v100
	v_sub_f32_e32 v17, v100, v173
	v_cmp_ge_f32_e32 vcc, s56, v17
	s_cmp_eq_u64 vcc, exec
	v_mov_b32_e32 v17, 1.0
	s_cbranch_scc0 .LBB0_469
	v_cmp_gt_f32_e32 vcc, 1.0, v17
	s_cbranch_vccz .LBB0_464

.LBB0_476:
	s_and_b64 vcc, exec, s[28:29]
	s_cbranch_vccz .LBB0_497
	global_load_dwordx4 v[114:117], v215, s[26:27]
	global_load_dwordx4 v[118:121], v215, s[26:27] offset:32
	v_lshl_add_u64 v[184:185], s[14:15], 0, v[168:169]
	v_add_co_u32_e32 v4, vcc, 0x2e0000, v184
	v_add_u32_e32 v66, 0, v165
	s_nop 0
	v_addc_co_u32_e32 v5, vcc, 0, v185, vcc
	global_load_dwordx4 v[122:125], v[184:185], off offset:2048
	global_load_dwordx4 v[150:153], v[184:185], off offset:1024
	global_load_dwordx4 v[154:157], v[4:5], off offset:2048
	global_load_dwordx4 v[158:161], v[4:5], off offset:1024
	global_load_dwordx4 v[126:129], v215, s[26:27] offset:64
	global_load_dwordx4 v[130:133], v215, s[26:27] offset:96
	global_load_dwordx4 v[134:137], v215, s[26:27] offset:128
	global_load_dwordx4 v[138:141], v215, s[26:27] offset:160
	global_load_dwordx4 v[142:145], v215, s[26:27] offset:192
	global_load_dwordx4 v[146:149], v215, s[26:27] offset:224
	v_add_u32_e32 v67, 0, v196
	v_add_u32_e32 v68, 0, v197
	v_add_u32_e32 v69, 0, v198
	v_add_u32_e32 v18, s36, v211
	v_mov_b32_e32 v16, v3
	v_mov_b32_e32 v17, v3
	v_add_u32_e32 v173, s37, v1
	v_mov_b32_e32 v2, v3
	v_mov_b32_e32 v4, v3
	v_mov_b32_e32 v5, v3
	v_mov_b32_e32 v6, v3
	v_mov_b32_e32 v7, v3
	v_mov_b32_e32 v8, v3
	v_mov_b32_e32 v9, v3
	v_mov_b32_e32 v10, v3
	v_mov_b32_e32 v11, v3
	v_mov_b32_e32 v12, v3
	v_mov_b32_e32 v13, v3
	v_mov_b32_e32 v14, v3
	v_mov_b32_e32 v15, v3
	v_subrev_u32_e32 v179, s35, v18
	v_mov_b64_e32 v[64:65], v[16:17]
	v_mov_b64_e32 v[48:49], v[16:17]
	v_mov_b64_e32 v[32:33], v[16:17]
	s_mov_b32 s8, 0
	v_mov_b32_e32 v181, 0
	v_mov_b32_e32 v175, 0xf149f2ca
	s_movk_i32 s30, 0x7f
	v_add_u32_e32 v177, 0x5f, v173
	v_mov_b64_e32 v[62:63], v[14:15]
	v_mov_b64_e32 v[60:61], v[12:13]
	v_mov_b64_e32 v[58:59], v[10:11]
	v_mov_b64_e32 v[56:57], v[8:9]
	v_mov_b64_e32 v[54:55], v[6:7]
	v_mov_b64_e32 v[52:53], v[4:5]
	v_mov_b64_e32 v[50:51], v[2:3]
	v_mov_b64_e32 v[46:47], v[14:15]
	v_mov_b64_e32 v[44:45], v[12:13]
	v_mov_b64_e32 v[42:43], v[10:11]
	v_mov_b64_e32 v[40:41], v[8:9]
	v_mov_b64_e32 v[38:39], v[6:7]
	v_mov_b64_e32 v[36:37], v[4:5]
	v_mov_b64_e32 v[34:35], v[2:3]
	v_mov_b64_e32 v[30:31], v[14:15]
	v_mov_b64_e32 v[28:29], v[12:13]
	v_mov_b64_e32 v[26:27], v[10:11]
	v_mov_b64_e32 v[24:25], v[8:9]
	v_mov_b64_e32 v[22:23], v[6:7]
	v_mov_b64_e32 v[20:21], v[4:5]
	v_mov_b64_e32 v[18:19], v[2:3]
	s_waitcnt vmcnt(9)
	ds_write_b128 v66, v[122:125]
	s_waitcnt vmcnt(7)
	ds_write_b128 v67, v[154:157]
	ds_write_b128 v68, v[150:153] offset:32768
	s_waitcnt vmcnt(6)
	ds_write_b128 v69, v[158:161] offset:32768
	v_mov_b64_e32 v[80:81], v[16:17]
	v_mov_b64_e32 v[78:79], v[14:15]
	v_mov_b64_e32 v[76:77], v[12:13]
	v_mov_b64_e32 v[74:75], v[10:11]
	v_mov_b64_e32 v[72:73], v[8:9]
	v_mov_b64_e32 v[70:71], v[6:7]
	v_mov_b64_e32 v[68:69], v[4:5]
	v_mov_b64_e32 v[66:67], v[2:3]
	s_waitcnt lgkmcnt(0)
	s_barrier
	s_waitcnt vmcnt(0)

.LBB0_480:
	s_and_b32 s79, s8, 1
	s_add_i32 s8, s30, 0xffffff81
	v_cmp_le_i32_e32 vcc, s8, v177
	v_cmp_ge_i32_e64 s[8:9], s30, v173
	s_and_b64 s[28:29], vcc, s[8:9]
	s_and_saveexec_b64 s[8:9], s[28:29]
	s_cbranch_execz .LBB0_487
	s_lshl_b32 s80, s79, 14
	s_add_i32 s28, s80, 0
	v_add3_u32 v2, s28, v200, v199
	ds_read_b128 v[4:7], v2 offset:32768
	ds_read_b128 v[224:227], v2 offset:40960
	v_add3_u32 v2, s28, v201, v199
	ds_read_b128 v[228:231], v2 offset:32768
	ds_read_b128 v[232:235], v2 offset:40960
	v_add_u32_e32 v11, 50, v179
	v_add_u32_e32 v13, 49, v179
	v_add_u32_e32 v15, 48, v179
	v_add_u32_e32 v17, 43, v179
	s_waitcnt lgkmcnt(3)
	v_mfma_f32_32x32x16_bf16 v[82:97], v[4:7], v[114:117], 0
	v_add3_u32 v2, s28, v202, v199
	ds_read_b128 v[4:7], v2 offset:32768
	s_waitcnt lgkmcnt(3)
	v_mfma_f32_32x32x16_bf16 v[98:113], v[224:227], v[114:117], 0
	ds_read_b128 v[224:227], v2 offset:40960
	s_waitcnt lgkmcnt(3)
	v_mfma_f32_32x32x16_bf16 v[82:97], v[228:231], v[118:121], v[82:97]
	v_add3_u32 v2, s28, v203, v199
	ds_read_b128 v[228:231], v2 offset:32768
	s_waitcnt lgkmcnt(3)
	v_mfma_f32_32x32x16_bf16 v[98:113], v[232:235], v[118:121], v[98:113]
	ds_read_b128 v[232:235], v2 offset:40960
	s_waitcnt lgkmcnt(3)
	v_mfma_f32_32x32x16_bf16 v[82:97], v[4:7], v[126:129], v[82:97]
	v_add3_u32 v2, s28, v204, v199
	ds_read_b128 v[4:7], v2 offset:32768
	s_waitcnt lgkmcnt(3)
	v_mfma_f32_32x32x16_bf16 v[98:113], v[224:227], v[126:129], v[98:113]
	ds_read_b128 v[224:227], v2 offset:40960
	s_waitcnt lgkmcnt(3)
	v_mfma_f32_32x32x16_bf16 v[82:97], v[228:231], v[130:133], v[82:97]
	v_add3_u32 v2, s28, v205, v199
	ds_read_b128 v[228:231], v2 offset:32768
	s_waitcnt lgkmcnt(3)
	v_mfma_f32_32x32x16_bf16 v[98:113], v[232:235], v[130:133], v[98:113]
	ds_read_b128 v[232:235], v2 offset:40960
	s_waitcnt lgkmcnt(3)
	v_mfma_f32_32x32x16_bf16 v[82:97], v[4:7], v[134:137], v[82:97]
	v_add3_u32 v2, s28, v206, v199
	ds_read_b128 v[4:7], v2 offset:32768
	s_waitcnt lgkmcnt(3)
	v_mfma_f32_32x32x16_bf16 v[98:113], v[224:227], v[134:137], v[98:113]
	ds_read_b128 v[224:227], v2 offset:40960
	s_waitcnt lgkmcnt(3)
	v_mfma_f32_32x32x16_bf16 v[82:97], v[228:231], v[138:141], v[82:97]
	v_add3_u32 v2, s28, v207, v199
	ds_read_b128 v[228:231], v2 offset:32768
	s_waitcnt lgkmcnt(3)
	v_mfma_f32_32x32x16_bf16 v[98:113], v[232:235], v[138:141], v[98:113]
	ds_read_b128 v[232:235], v2 offset:40960
	s_waitcnt lgkmcnt(3)
	v_mfma_f32_32x32x16_bf16 v[82:97], v[4:7], v[142:145], v[82:97]
	s_waitcnt lgkmcnt(2)
	v_mfma_f32_32x32x16_bf16 v[98:113], v[224:227], v[142:145], v[98:113]
	s_waitcnt lgkmcnt(1)
	v_mfma_f32_32x32x16_bf16 v[82:97], v[228:231], v[146:149], v[82:97]
	v_add_u32_e32 v2, 59, v179
	v_cmp_lt_u32_e32 vcc, s55, v2
	v_add_u32_e32 v2, 27, v179
	v_add_u32_e32 v4, 58, v179
	s_nop 7
	v_cndmask_b32_e32 v5, v220, v82, vcc
	s_waitcnt lgkmcnt(0)
	v_mfma_f32_32x32x16_bf16 v[98:113], v[232:235], v[146:149], v[98:113]
	v_cmp_lt_u32_e32 vcc, s55, v2
	v_add_u32_e32 v6, 57, v179
	v_add_u32_e32 v7, 56, v179
	v_add_u32_e32 v9, 51, v179
	s_nop 7
	v_cndmask_b32_e32 v2, v220, v98, vcc
	v_cmp_lt_u32_e32 vcc, s55, v4
	v_add_u32_e32 v4, 26, v179
	s_nop 0
	v_cndmask_b32_e32 v8, v220, v83, vcc
	v_cmp_lt_u32_e32 vcc, s55, v4
	s_nop 1
	v_cndmask_b32_e32 v4, v220, v99, vcc
	v_cmp_lt_u32_e32 vcc, s55, v6
	v_add_u32_e32 v6, 25, v179
	s_nop 0
	v_cndmask_b32_e32 v10, v220, v84, vcc
	v_cmp_lt_u32_e32 vcc, s55, v6
	s_nop 1
	v_cndmask_b32_e32 v6, v220, v100, vcc
	v_cmp_lt_u32_e32 vcc, s55, v7
	v_add_u32_e32 v7, 24, v179
	v_max_f32_e32 v100, v5, v5
	v_cndmask_b32_e32 v12, v220, v85, vcc
	v_cmp_lt_u32_e32 vcc, s55, v7
	s_nop 1
	v_cndmask_b32_e32 v7, v220, v101, vcc
	v_cmp_lt_u32_e32 vcc, s55, v9
	v_add_u32_e32 v9, 19, v179
	s_nop 0
	v_cndmask_b32_e32 v14, v220, v86, vcc
	v_cmp_lt_u32_e32 vcc, s55, v9
	s_nop 1
	v_cndmask_b32_e32 v9, v220, v102, vcc
	v_cmp_lt_u32_e32 vcc, s55, v11
	v_add_u32_e32 v11, 18, v179
	s_nop 0
	v_cndmask_b32_e32 v16, v220, v87, vcc
	v_cmp_lt_u32_e32 vcc, s55, v11
	s_nop 1
	v_cndmask_b32_e32 v11, v220, v103, vcc
	v_cmp_lt_u32_e32 vcc, s55, v13
	v_add_u32_e32 v13, 17, v179
	s_nop 0
	v_cndmask_b32_e32 v83, v220, v88, vcc
	v_cmp_lt_u32_e32 vcc, s55, v13
	s_nop 1
	v_cndmask_b32_e32 v13, v220, v104, vcc
	v_cmp_lt_u32_e32 vcc, s55, v15
	v_add_u32_e32 v15, 16, v179
	s_nop 0
	v_cndmask_b32_e32 v85, v220, v89, vcc
	v_cmp_lt_u32_e32 vcc, s55, v15
	s_nop 1
	v_cndmask_b32_e32 v15, v220, v105, vcc
	v_cmp_lt_u32_e32 vcc, s55, v17
	v_add_u32_e32 v17, 11, v179
	s_nop 0
	v_cndmask_b32_e32 v87, v220, v90, vcc
	v_cmp_lt_u32_e32 vcc, s55, v17
	v_add_u32_e32 v17, 42, v179
	s_nop 0
	v_cndmask_b32_e32 v82, v220, v106, vcc
	v_cmp_lt_u32_e32 vcc, s55, v17
	v_add_u32_e32 v17, 10, v179
	s_nop 0
	v_cndmask_b32_e32 v89, v220, v91, vcc
	v_cmp_lt_u32_e32 vcc, s55, v17
	v_add_u32_e32 v17, 41, v179
	s_nop 0
	v_cndmask_b32_e32 v84, v220, v107, vcc
	v_cmp_lt_u32_e32 vcc, s55, v17
	v_add_u32_e32 v17, 9, v179
	s_nop 0
	v_cndmask_b32_e32 v91, v220, v92, vcc
	v_cmp_lt_u32_e32 vcc, s55, v17
	v_add_u32_e32 v17, 40, v179
	s_nop 0
	v_cndmask_b32_e32 v86, v220, v108, vcc
	v_cmp_lt_u32_e32 vcc, s55, v17
	v_add_u32_e32 v17, 8, v179
	s_nop 0
	v_cndmask_b32_e32 v93, v220, v93, vcc
	v_cmp_lt_u32_e32 vcc, s55, v17
	v_add_u32_e32 v17, 35, v179
	s_nop 0
	v_cndmask_b32_e32 v88, v220, v109, vcc
	v_cmp_lt_u32_e32 vcc, s55, v17
	v_add_u32_e32 v17, 3, v179
	s_nop 0
	v_cndmask_b32_e32 v98, v220, v94, vcc
	v_cmp_lt_u32_e32 vcc, s55, v17
	v_add_u32_e32 v17, 34, v179
	s_nop 0
	v_cndmask_b32_e32 v90, v220, v110, vcc
	v_cmp_lt_u32_e32 vcc, s55, v17
	v_add_u32_e32 v17, 2, v179
	s_nop 0
	v_cndmask_b32_e32 v99, v220, v95, vcc
	v_cmp_lt_u32_e32 vcc, s55, v17
	v_add_u32_e32 v17, 33, v179
	s_nop 0
	v_cndmask_b32_e32 v92, v220, v111, vcc
	v_cmp_lt_u32_e32 vcc, s55, v17
	v_add_u32_e32 v17, 1, v179
	s_nop 0
	v_cndmask_b32_e32 v96, v220, v96, vcc
	v_cmp_lt_u32_e32 vcc, s55, v17
	v_add_u32_e32 v17, 32, v179
	s_nop 0
	v_cndmask_b32_e32 v94, v220, v112, vcc
	v_cmp_lt_u32_e32 vcc, s55, v17
	v_max_f32_e32 v17, v8, v8
	v_max_f32_e32 v17, v100, v17
	v_max3_f32 v17, v17, v10, v12
	v_max3_f32 v17, v17, v14, v16
	v_max3_f32 v17, v17, v83, v85
	v_max3_f32 v17, v17, v87, v89
	v_max3_f32 v17, v17, v91, v93
	v_cndmask_b32_e32 v97, v220, v97, vcc
	v_max3_f32 v17, v17, v98, v99
	v_max3_f32 v17, v17, v96, v97
	v_max3_f32 v17, v17, v2, v4
	v_max3_f32 v17, v17, v6, v7
	v_max3_f32 v17, v17, v9, v11
	v_max3_f32 v17, v17, v13, v15
	v_max3_f32 v17, v17, v82, v84
	v_cmp_lt_u32_e32 vcc, s55, v179
	v_max3_f32 v17, v17, v86, v88
	v_max3_f32 v17, v17, v90, v92
	v_cndmask_b32_e32 v95, v220, v113, vcc
	v_max3_f32 v17, v17, v94, v95
	v_mov_b32_e32 v100, v17
	s_nop 1
	v_permlane32_swap_b32_e32 v17, v100
	v_max_f32_e32 v100, v100, v100
	v_max_f32_e32 v17, v17, v17
	v_max_f32_e32 v100, v17, v100
	v_sub_f32_e32 v17, v100, v175
	v_cmp_ge_f32_e32 vcc, s56, v17
	s_cmp_eq_u64 vcc, exec
	v_mov_b32_e32 v17, 1.0
	s_cbranch_scc0 .LBB0_491
	v_cmp_gt_f32_e32 vcc, 1.0, v17
	s_cbranch_vccz .LBB0_486

.LBB0_498:
	s_mul_i32 s76, s76, 0x5c0000
	s_add_u32 s8, s77, s76
	s_addc_u32 s9, s78, 0
	global_load_dwordx4 v[114:117], v217, s[8:9]
	global_load_dwordx4 v[118:121], v217, s[8:9] offset:32
	v_lshl_add_u64 v[184:185], s[14:15], 0, v[170:171]
	v_add_co_u32_e32 v4, vcc, s74, v184
	v_add_u32_e32 v66, 0, v165
	s_nop 0
	v_addc_co_u32_e32 v5, vcc, 0, v185, vcc
	global_load_dwordx4 v[122:125], v[184:185], off offset:2048
	global_load_dwordx4 v[150:153], v[184:185], off offset:1024
	global_load_dwordx4 v[154:157], v[4:5], off offset:2048
	global_load_dwordx4 v[158:161], v[4:5], off offset:1024
	global_load_dwordx4 v[126:129], v217, s[8:9] offset:64
	global_load_dwordx4 v[130:133], v217, s[8:9] offset:96
	global_load_dwordx4 v[134:137], v217, s[8:9] offset:128
	global_load_dwordx4 v[138:141], v217, s[8:9] offset:160
	global_load_dwordx4 v[142:145], v217, s[8:9] offset:192
	global_load_dwordx4 v[146:149], v217, s[8:9] offset:224
	v_add_u32_e32 v67, 0, v196
	v_add_u32_e32 v68, 0, v197
	v_add_u32_e32 v69, 0, v198
	v_add_u32_e32 v18, s36, v211
	v_mov_b32_e32 v16, v3
	v_mov_b32_e32 v17, v3
	v_add_u32_e32 v173, s37, v1
	v_mov_b32_e32 v2, v3
	v_mov_b32_e32 v4, v3
	v_mov_b32_e32 v5, v3
	v_mov_b32_e32 v6, v3
	v_mov_b32_e32 v7, v3
	v_mov_b32_e32 v8, v3
	v_mov_b32_e32 v9, v3
	v_mov_b32_e32 v10, v3
	v_mov_b32_e32 v11, v3
	v_mov_b32_e32 v12, v3
	v_mov_b32_e32 v13, v3
	v_mov_b32_e32 v14, v3
	v_mov_b32_e32 v15, v3
	v_subrev_u32_e32 v179, s35, v18
	v_mov_b64_e32 v[64:65], v[16:17]
	v_mov_b64_e32 v[48:49], v[16:17]
	v_mov_b64_e32 v[32:33], v[16:17]
	s_mov_b32 s8, 0
	v_mov_b32_e32 v181, 0
	v_mov_b32_e32 v175, 0xf149f2ca
	s_movk_i32 s28, 0x7f
	v_add_u32_e32 v177, 0x5f, v173
	v_mov_b64_e32 v[62:63], v[14:15]
	v_mov_b64_e32 v[60:61], v[12:13]
	v_mov_b64_e32 v[58:59], v[10:11]
	v_mov_b64_e32 v[56:57], v[8:9]
	v_mov_b64_e32 v[54:55], v[6:7]
	v_mov_b64_e32 v[52:53], v[4:5]
	v_mov_b64_e32 v[50:51], v[2:3]
	v_mov_b64_e32 v[46:47], v[14:15]
	v_mov_b64_e32 v[44:45], v[12:13]
	v_mov_b64_e32 v[42:43], v[10:11]
	v_mov_b64_e32 v[40:41], v[8:9]
	v_mov_b64_e32 v[38:39], v[6:7]
	v_mov_b64_e32 v[36:37], v[4:5]
	v_mov_b64_e32 v[34:35], v[2:3]
	v_mov_b64_e32 v[30:31], v[14:15]
	v_mov_b64_e32 v[28:29], v[12:13]
	v_mov_b64_e32 v[26:27], v[10:11]
	v_mov_b64_e32 v[24:25], v[8:9]
	v_mov_b64_e32 v[22:23], v[6:7]
	v_mov_b64_e32 v[20:21], v[4:5]
	v_mov_b64_e32 v[18:19], v[2:3]
	s_waitcnt vmcnt(9)
	ds_write_b128 v66, v[122:125]
	s_waitcnt vmcnt(7)
	ds_write_b128 v67, v[154:157]
	ds_write_b128 v68, v[150:153] offset:32768
	s_waitcnt vmcnt(6)
	ds_write_b128 v69, v[158:161] offset:32768
	v_mov_b64_e32 v[80:81], v[16:17]
	v_mov_b64_e32 v[78:79], v[14:15]
	v_mov_b64_e32 v[76:77], v[12:13]
	v_mov_b64_e32 v[74:75], v[10:11]
	v_mov_b64_e32 v[72:73], v[8:9]
	v_mov_b64_e32 v[70:71], v[6:7]
	v_mov_b64_e32 v[68:69], v[4:5]
	v_mov_b64_e32 v[66:67], v[2:3]
	s_waitcnt lgkmcnt(0)
	s_barrier
	s_waitcnt vmcnt(0)

.LBB0_501:
	s_and_b32 s30, s8, 1
	s_add_i32 s8, s28, 0xffffff81
	v_cmp_le_i32_e32 vcc, s8, v177
	v_cmp_ge_i32_e64 s[8:9], s28, v173
	s_and_b64 s[26:27], vcc, s[8:9]
	s_and_saveexec_b64 s[8:9], s[26:27]
	s_cbranch_execz .LBB0_508
	s_lshl_b32 s31, s30, 14
	s_add_i32 s26, s31, 0
	v_add3_u32 v2, s26, v200, v199
	ds_read_b128 v[4:7], v2 offset:32768
	ds_read_b128 v[8:11], v2 offset:40960
	v_add3_u32 v2, s26, v201, v199
	v_add_u32_e32 v13, 49, v179
	v_add_u32_e32 v15, 48, v179
	s_waitcnt lgkmcnt(1)
	v_mfma_f32_32x32x16_bf16 v[82:97], v[4:7], v[114:117], 0
	v_add_u32_e32 v17, 43, v179
	s_waitcnt lgkmcnt(0)
	v_mfma_f32_32x32x16_bf16 v[98:113], v[8:11], v[114:117], 0
	ds_read_b128 v[4:7], v2 offset:32768
	ds_read_b128 v[8:11], v2 offset:40960
	v_add3_u32 v2, s26, v202, v199
	s_waitcnt lgkmcnt(1)
	v_mfma_f32_32x32x16_bf16 v[82:97], v[4:7], v[118:121], v[82:97]
	s_waitcnt lgkmcnt(0)
	v_mfma_f32_32x32x16_bf16 v[98:113], v[8:11], v[118:121], v[98:113]
	ds_read_b128 v[4:7], v2 offset:32768
	ds_read_b128 v[8:11], v2 offset:40960
	v_add3_u32 v2, s26, v203, v199
	s_waitcnt lgkmcnt(1)
	v_mfma_f32_32x32x16_bf16 v[82:97], v[4:7], v[126:129], v[82:97]
	s_waitcnt lgkmcnt(0)
	v_mfma_f32_32x32x16_bf16 v[98:113], v[8:11], v[126:129], v[98:113]
	ds_read_b128 v[4:7], v2 offset:32768
	ds_read_b128 v[8:11], v2 offset:40960
	v_add3_u32 v2, s26, v204, v199
	s_waitcnt lgkmcnt(1)
	v_mfma_f32_32x32x16_bf16 v[82:97], v[4:7], v[130:133], v[82:97]
	s_waitcnt lgkmcnt(0)
	v_mfma_f32_32x32x16_bf16 v[98:113], v[8:11], v[130:133], v[98:113]
	ds_read_b128 v[4:7], v2 offset:32768
	ds_read_b128 v[8:11], v2 offset:40960
	v_add3_u32 v2, s26, v205, v199
	s_waitcnt lgkmcnt(1)
	v_mfma_f32_32x32x16_bf16 v[82:97], v[4:7], v[134:137], v[82:97]
	s_waitcnt lgkmcnt(0)
	v_mfma_f32_32x32x16_bf16 v[98:113], v[8:11], v[134:137], v[98:113]
	ds_read_b128 v[4:7], v2 offset:32768
	ds_read_b128 v[8:11], v2 offset:40960
	v_add3_u32 v2, s26, v206, v199
	s_waitcnt lgkmcnt(1)
	v_mfma_f32_32x32x16_bf16 v[82:97], v[4:7], v[138:141], v[82:97]
	s_waitcnt lgkmcnt(0)
	v_mfma_f32_32x32x16_bf16 v[98:113], v[8:11], v[138:141], v[98:113]
	ds_read_b128 v[4:7], v2 offset:32768
	ds_read_b128 v[8:11], v2 offset:40960
	v_add3_u32 v2, s26, v207, v199
	s_waitcnt lgkmcnt(1)
	v_mfma_f32_32x32x16_bf16 v[82:97], v[4:7], v[142:145], v[82:97]
	s_waitcnt lgkmcnt(0)
	v_mfma_f32_32x32x16_bf16 v[98:113], v[8:11], v[142:145], v[98:113]
	ds_read_b128 v[4:7], v2 offset:32768
	ds_read_b128 v[8:11], v2 offset:40960
	v_add_u32_e32 v2, 59, v179
	v_cmp_lt_u32_e32 vcc, s55, v2
	v_add_u32_e32 v2, 27, v179
	s_waitcnt lgkmcnt(1)
	v_mfma_f32_32x32x16_bf16 v[82:97], v[4:7], v[146:149], v[82:97]
	v_add_u32_e32 v4, 58, v179
	v_add_u32_e32 v6, 57, v179
	v_add_u32_e32 v7, 56, v179
	s_waitcnt lgkmcnt(0)
	v_mfma_f32_32x32x16_bf16 v[98:113], v[8:11], v[146:149], v[98:113]
	s_nop 6
	v_cndmask_b32_e32 v5, v220, v82, vcc
	v_cmp_lt_u32_e32 vcc, s55, v2
	v_add_u32_e32 v9, 51, v179
	v_add_u32_e32 v11, 50, v179
	s_nop 0
	v_cndmask_b32_e32 v2, v220, v98, vcc
	v_cmp_lt_u32_e32 vcc, s55, v4
	v_add_u32_e32 v4, 26, v179
	s_nop 0
	v_cndmask_b32_e32 v8, v220, v83, vcc
	v_cmp_lt_u32_e32 vcc, s55, v4
	s_nop 1
	v_cndmask_b32_e32 v4, v220, v99, vcc
	v_cmp_lt_u32_e32 vcc, s55, v6
	v_add_u32_e32 v6, 25, v179
	s_nop 0
	v_cndmask_b32_e32 v10, v220, v84, vcc
	v_cmp_lt_u32_e32 vcc, s55, v6
	s_nop 1
	v_cndmask_b32_e32 v6, v220, v100, vcc
	v_cmp_lt_u32_e32 vcc, s55, v7
	v_add_u32_e32 v7, 24, v179
	v_max_f32_e32 v100, v5, v5
	v_cndmask_b32_e32 v12, v220, v85, vcc
	v_cmp_lt_u32_e32 vcc, s55, v7
	s_nop 1
	v_cndmask_b32_e32 v7, v220, v101, vcc
	v_cmp_lt_u32_e32 vcc, s55, v9
	v_add_u32_e32 v9, 19, v179
	s_nop 0
	v_cndmask_b32_e32 v14, v220, v86, vcc
	v_cmp_lt_u32_e32 vcc, s55, v9
	s_nop 1
	v_cndmask_b32_e32 v9, v220, v102, vcc
	v_cmp_lt_u32_e32 vcc, s55, v11
	v_add_u32_e32 v11, 18, v179
	s_nop 0
	v_cndmask_b32_e32 v16, v220, v87, vcc
	v_cmp_lt_u32_e32 vcc, s55, v11
	s_nop 1
	v_cndmask_b32_e32 v11, v220, v103, vcc
	v_cmp_lt_u32_e32 vcc, s55, v13
	v_add_u32_e32 v13, 17, v179
	s_nop 0
	v_cndmask_b32_e32 v83, v220, v88, vcc
	v_cmp_lt_u32_e32 vcc, s55, v13
	s_nop 1
	v_cndmask_b32_e32 v13, v220, v104, vcc
	v_cmp_lt_u32_e32 vcc, s55, v15
	v_add_u32_e32 v15, 16, v179
	s_nop 0
	v_cndmask_b32_e32 v85, v220, v89, vcc
	v_cmp_lt_u32_e32 vcc, s55, v15
	s_nop 1
	v_cndmask_b32_e32 v15, v220, v105, vcc
	v_cmp_lt_u32_e32 vcc, s55, v17
	v_add_u32_e32 v17, 11, v179
	s_nop 0
	v_cndmask_b32_e32 v87, v220, v90, vcc
	v_cmp_lt_u32_e32 vcc, s55, v17
	v_add_u32_e32 v17, 42, v179
	s_nop 0
	v_cndmask_b32_e32 v82, v220, v106, vcc
	v_cmp_lt_u32_e32 vcc, s55, v17
	v_add_u32_e32 v17, 10, v179
	s_nop 0
	v_cndmask_b32_e32 v89, v220, v91, vcc
	v_cmp_lt_u32_e32 vcc, s55, v17
	v_add_u32_e32 v17, 41, v179
	s_nop 0
	v_cndmask_b32_e32 v84, v220, v107, vcc
	v_cmp_lt_u32_e32 vcc, s55, v17
	v_add_u32_e32 v17, 9, v179
	s_nop 0
	v_cndmask_b32_e32 v91, v220, v92, vcc
	v_cmp_lt_u32_e32 vcc, s55, v17
	v_add_u32_e32 v17, 40, v179
	s_nop 0
	v_cndmask_b32_e32 v86, v220, v108, vcc
	v_cmp_lt_u32_e32 vcc, s55, v17
	v_add_u32_e32 v17, 8, v179
	s_nop 0
	v_cndmask_b32_e32 v93, v220, v93, vcc
	v_cmp_lt_u32_e32 vcc, s55, v17
	v_add_u32_e32 v17, 35, v179
	s_nop 0
	v_cndmask_b32_e32 v88, v220, v109, vcc
	v_cmp_lt_u32_e32 vcc, s55, v17
	v_add_u32_e32 v17, 3, v179
	s_nop 0
	v_cndmask_b32_e32 v98, v220, v94, vcc
	v_cmp_lt_u32_e32 vcc, s55, v17
	v_add_u32_e32 v17, 34, v179
	s_nop 0
	v_cndmask_b32_e32 v90, v220, v110, vcc
	v_cmp_lt_u32_e32 vcc, s55, v17
	v_add_u32_e32 v17, 2, v179
	s_nop 0
	v_cndmask_b32_e32 v99, v220, v95, vcc
	v_cmp_lt_u32_e32 vcc, s55, v17
	v_add_u32_e32 v17, 33, v179
	s_nop 0
	v_cndmask_b32_e32 v92, v220, v111, vcc
	v_cmp_lt_u32_e32 vcc, s55, v17
	v_add_u32_e32 v17, 1, v179
	s_nop 0
	v_cndmask_b32_e32 v96, v220, v96, vcc
	v_cmp_lt_u32_e32 vcc, s55, v17
	v_add_u32_e32 v17, 32, v179
	s_nop 0
	v_cndmask_b32_e32 v94, v220, v112, vcc
	v_cmp_lt_u32_e32 vcc, s55, v17
	v_max_f32_e32 v17, v8, v8
	v_max_f32_e32 v17, v100, v17
	v_max3_f32 v17, v17, v10, v12
	v_max3_f32 v17, v17, v14, v16
	v_max3_f32 v17, v17, v83, v85
	v_max3_f32 v17, v17, v87, v89
	v_max3_f32 v17, v17, v91, v93
	v_cndmask_b32_e32 v97, v220, v97, vcc
	v_max3_f32 v17, v17, v98, v99
	v_max3_f32 v17, v17, v96, v97
	v_max3_f32 v17, v17, v2, v4
	v_max3_f32 v17, v17, v6, v7
	v_max3_f32 v17, v17, v9, v11
	v_max3_f32 v17, v17, v13, v15
	v_max3_f32 v17, v17, v82, v84
	v_cmp_lt_u32_e32 vcc, s55, v179
	v_max3_f32 v17, v17, v86, v88
	v_max3_f32 v17, v17, v90, v92
	v_cndmask_b32_e32 v95, v220, v113, vcc
	v_max3_f32 v17, v17, v94, v95
	v_mov_b32_e32 v100, v17
	s_nop 1
	v_permlane32_swap_b32_e32 v17, v100
	v_max_f32_e32 v100, v100, v100
	v_max_f32_e32 v17, v17, v17
	v_max_f32_e32 v100, v17, v100
	v_sub_f32_e32 v17, v100, v175
	v_cmp_ge_f32_e32 vcc, s56, v17
	s_cmp_eq_u64 vcc, exec
	v_mov_b32_e32 v17, 1.0
	s_cbranch_scc0 .LBB0_512
	v_cmp_gt_f32_e32 vcc, 1.0, v17
	s_cbranch_vccz .LBB0_507
